# proj and MLP2: the 10 harmless re-read LDS-DMA loads of the last K-loop iteration are skipped, vmcnt(0) drains instead
# baseline (speedup 1.0000x reference)
.LBB4_22:
	s_add_u32 s34, s26, s30
	s_addc_u32 s35, s27, s31
	s_add_u32 s34, s34, 0x180
	s_addc_u32 s35, s35, 0
	s_add_u32 s68, s28, s30
	s_addc_u32 s69, s29, s31
	s_add_u32 s70, s68, 0x180
	s_addc_u32 s71, s69, 0
	s_cmp_eq_u32 s60, s67
	s_cselect_b32 s69, s5, s35
	s_cselect_b32 s68, s4, s34
	s_cselect_b32 s35, s7, s71
	s_cselect_b32 s34, s6, s70
	s_cselect_b32 s73, 1, 0
	s_add_i32 s70, s62, s44
	v_lshl_add_u64 v[108:109], v[98:99], 0, s[30:31]
	s_mov_b32 m0, s70
	ds_read_b128 v[130:133], v136 offset:16384
	ds_read_b128 v[142:145], v136 offset:17408
	ds_read_b128 v[146:149], v136 offset:18432
	ds_read_b128 v[150:153], v136 offset:19456
	ds_read_b128 v[154:157], v137
	ds_read_b128 v[158:161], v137 offset:1024
	ds_read_b128 v[162:165], v137 offset:2048
	ds_read_b128 v[166:169], v137 offset:3072
	ds_read_b128 v[170:173], v137 offset:4096
	ds_read_b128 v[174:177], v137 offset:5120
	ds_read_b128 v[178:181], v137 offset:6144
	ds_read_b128 v[182:185], v137 offset:7168
	global_load_lds_dwordx4 v[108:109], off
	v_lshl_add_u64 v[108:109], v[100:101], 0, s[30:31]
	s_add_i32 m0, s70, 0x2000
	s_nop 0
	global_load_lds_dwordx4 v[108:109], off
	s_barrier
	s_waitcnt lgkmcnt(0)
	s_setprio 1
	s_waitcnt lgkmcnt(0)
	v_mfma_f32_16x16x32_f16 v[94:97], v[130:133], v[154:157], v[94:97]
	v_mfma_f32_16x16x32_f16 v[90:93], v[146:149], v[154:157], v[90:93]
	v_mfma_f32_16x16x32_f16 v[82:85], v[130:133], v[162:165], v[82:85]
	v_mfma_f32_16x16x32_f16 v[78:81], v[146:149], v[162:165], v[78:81]
	v_mfma_f32_16x16x32_f16 v[70:73], v[130:133], v[170:173], v[70:73]
	v_mfma_f32_16x16x32_f16 v[66:69], v[146:149], v[170:173], v[66:69]
	v_mfma_f32_16x16x32_f16 v[58:61], v[130:133], v[178:181], v[58:61]
	v_mfma_f32_16x16x32_f16 v[54:57], v[146:149], v[178:181], v[54:57]
	v_mfma_f32_16x16x32_f16 v[94:97], v[142:145], v[158:161], v[94:97]
	v_mfma_f32_16x16x32_f16 v[90:93], v[150:153], v[158:161], v[90:93]
	v_mfma_f32_16x16x32_f16 v[82:85], v[142:145], v[166:169], v[82:85]
	v_mfma_f32_16x16x32_f16 v[78:81], v[150:153], v[166:169], v[78:81]
	v_mfma_f32_16x16x32_f16 v[70:73], v[142:145], v[174:177], v[70:73]
	v_mfma_f32_16x16x32_f16 v[66:69], v[150:153], v[174:177], v[66:69]
	v_mfma_f32_16x16x32_f16 v[58:61], v[142:145], v[182:185], v[58:61]
	v_mfma_f32_16x16x32_f16 v[54:57], v[150:153], v[182:185], v[54:57]
	s_setprio 0
	s_barrier
	v_lshl_add_u64 v[108:109], v[102:103], 0, s[30:31]
	s_add_i32 m0, s49, 0x18000
	ds_read_b128 v[130:133], v136 offset:20480
	ds_read_b128 v[142:145], v136 offset:21504
	global_load_lds_dwordx4 v[108:109], off
	v_lshl_add_u64 v[108:109], v[104:105], 0, s[30:31]
	s_add_i32 m0, s49, 0x1a000
	s_nop 0
	global_load_lds_dwordx4 v[108:109], off
	v_lshl_add_u64 v[108:109], v[106:107], 0, s[30:31]
	s_add_i32 m0, s49, 0x1c000
	s_nop 0
	global_load_lds_dwordx4 v[108:109], off
	s_cmp_lg_u32 s67, 0
	s_cbranch_scc1 .Lpj_norm_0
	s_mul_i32 s72, s66, 0xc0
	v_add_u32_e32 v214, s72, v135
	v_ashrrev_i32_e32 v215, 31, v214
	v_lshl_add_u64 v[214:215], v[214:215], 2, s[10:11]
	global_load_dwordx4 v[202:205], v[214:215], off
	global_load_dwordx4 v[206:209], v[214:215], off offset:64
	global_load_dwordx4 v[210:213], v[214:215], off offset:128
	global_load_dwordx4 v[2:5], v[194:195], off
	global_load_dwordx4 v[6:9], v[194:195], off offset:64
	global_load_dwordx4 v[10:13], v[194:195], off offset:128
	global_load_dwordx4 v[14:17], v[196:197], off
	s_waitcnt vmcnt(12)
	s_branch .Lpj_join_0

.Lpj_join_0:
	s_barrier
	s_waitcnt lgkmcnt(0)
	s_setprio 1
	s_waitcnt lgkmcnt(0)
	v_mfma_f32_16x16x32_f16 v[86:89], v[130:133], v[154:157], v[86:89]
	v_mfma_f32_16x16x32_f16 v[74:77], v[130:133], v[162:165], v[74:77]
	v_mfma_f32_16x16x32_f16 v[62:65], v[130:133], v[170:173], v[62:65]
	v_mfma_f32_16x16x32_f16 v[50:53], v[130:133], v[178:181], v[50:53]
	v_mfma_f32_16x16x32_f16 v[86:89], v[142:145], v[158:161], v[86:89]
	v_mfma_f32_16x16x32_f16 v[74:77], v[142:145], v[166:169], v[74:77]
	v_mfma_f32_16x16x32_f16 v[62:65], v[142:145], v[174:177], v[62:65]
	v_mfma_f32_16x16x32_f16 v[50:53], v[142:145], v[182:185], v[50:53]
	s_setprio 0
	s_barrier
	s_mov_b32 m0, s49
	v_lshl_add_u64 v[108:109], s[68:69], 0, v[110:111]
	ds_read_b128 v[130:133], v136 offset:57344
	ds_read_b128 v[142:145], v136 offset:58368
	ds_read_b128 v[146:149], v136 offset:59392
	ds_read_b128 v[150:153], v136 offset:60416
	ds_read_b128 v[154:157], v137 offset:40960
	ds_read_b128 v[158:161], v137 offset:41984
	ds_read_b128 v[162:165], v137 offset:43008
	ds_read_b128 v[166:169], v137 offset:44032
	ds_read_b128 v[170:173], v137 offset:45056
	ds_read_b128 v[174:177], v137 offset:46080
	ds_read_b128 v[178:181], v137 offset:47104
	ds_read_b128 v[182:185], v137 offset:48128
	s_cmp_eq_u32 s73, 1
	s_cbranch_scc1 .Lnd_proj_0
	global_load_lds_dwordx4 v[108:109], off
	v_lshl_add_u64 v[186:187], s[68:69], 0, v[114:115]
	s_mov_b32 m0, s50
	s_nop 0
	global_load_lds_dwordx4 v[186:187], off
.Lnd_proj_0:
	s_barrier
	s_waitcnt lgkmcnt(0)
	s_setprio 1
	s_waitcnt lgkmcnt(0)
	v_mfma_f32_16x16x32_f16 v[94:97], v[130:133], v[154:157], v[94:97]
	v_mfma_f32_16x16x32_f16 v[90:93], v[146:149], v[154:157], v[90:93]
	v_mfma_f32_16x16x32_f16 v[82:85], v[130:133], v[162:165], v[82:85]
	v_mfma_f32_16x16x32_f16 v[78:81], v[146:149], v[162:165], v[78:81]
	v_mfma_f32_16x16x32_f16 v[70:73], v[130:133], v[170:173], v[70:73]
	v_mfma_f32_16x16x32_f16 v[66:69], v[146:149], v[170:173], v[66:69]
	v_mfma_f32_16x16x32_f16 v[58:61], v[130:133], v[178:181], v[58:61]
	v_mfma_f32_16x16x32_f16 v[54:57], v[146:149], v[178:181], v[54:57]
	v_mfma_f32_16x16x32_f16 v[94:97], v[142:145], v[158:161], v[94:97]
	v_mfma_f32_16x16x32_f16 v[90:93], v[150:153], v[158:161], v[90:93]
	v_mfma_f32_16x16x32_f16 v[82:85], v[142:145], v[166:169], v[82:85]
	v_mfma_f32_16x16x32_f16 v[78:81], v[150:153], v[166:169], v[78:81]
	v_mfma_f32_16x16x32_f16 v[70:73], v[142:145], v[174:177], v[70:73]
	v_mfma_f32_16x16x32_f16 v[66:69], v[150:153], v[174:177], v[66:69]
	v_mfma_f32_16x16x32_f16 v[58:61], v[142:145], v[182:185], v[58:61]
	v_mfma_f32_16x16x32_f16 v[54:57], v[150:153], v[182:185], v[54:57]
	s_setprio 0
	s_barrier
	s_mov_b32 m0, s51
	v_lshl_add_u64 v[188:189], s[34:35], 0, v[112:113]
	ds_read_b128 v[130:133], v136 offset:61440
	ds_read_b128 v[142:145], v136 offset:62464
	s_cmp_eq_u32 s73, 1
	s_cbranch_scc1 .Lnd_proj_1
	global_load_lds_dwordx4 v[188:189], off
	v_lshl_add_u64 v[190:191], s[34:35], 0, v[116:117]
	s_mov_b32 m0, s52
	v_lshl_add_u64 v[192:193], s[34:35], 0, v[118:119]
	global_load_lds_dwordx4 v[190:191], off
	s_mov_b32 m0, s53
	s_nop 0
	global_load_lds_dwordx4 v[192:193], off
.Lnd_proj_1b:
	s_cmp_lg_u32 s67, 0
	s_cbranch_scc1 .Lpj_norm_1
	global_load_dwordx4 v[18:21], v[196:197], off offset:64
	global_load_dwordx4 v[22:25], v[196:197], off offset:128
	global_load_dwordx4 v[26:29], v[198:199], off
	global_load_dwordx4 v[30:33], v[198:199], off offset:64
	s_waitcnt vmcnt(16)
	s_branch .Lpj_join_1

.Lpj_join_1:
	s_barrier
	s_waitcnt lgkmcnt(0)
	s_setprio 1
	s_waitcnt lgkmcnt(0)
	v_mfma_f32_16x16x32_f16 v[86:89], v[130:133], v[154:157], v[86:89]
	v_mfma_f32_16x16x32_f16 v[74:77], v[130:133], v[162:165], v[74:77]
	v_mfma_f32_16x16x32_f16 v[62:65], v[130:133], v[170:173], v[62:65]
	v_mfma_f32_16x16x32_f16 v[50:53], v[130:133], v[178:181], v[50:53]
	v_mfma_f32_16x16x32_f16 v[86:89], v[142:145], v[158:161], v[86:89]
	v_mfma_f32_16x16x32_f16 v[74:77], v[142:145], v[166:169], v[74:77]
	v_mfma_f32_16x16x32_f16 v[62:65], v[142:145], v[174:177], v[62:65]
	v_mfma_f32_16x16x32_f16 v[50:53], v[142:145], v[182:185], v[50:53]
	s_setprio 0
	s_barrier
	s_mov_b32 m0, s56
	v_lshl_add_u64 v[108:109], v[108:109], 0, s[22:23]
	ds_read_b128 v[130:133], v138
	ds_read_b128 v[142:145], v138 offset:1024
	ds_read_b128 v[146:149], v138 offset:2048
	ds_read_b128 v[150:153], v138 offset:3072
	ds_read_b128 v[154:157], v139
	ds_read_b128 v[158:161], v139 offset:1024
	ds_read_b128 v[162:165], v139 offset:2048
	ds_read_b128 v[166:169], v139 offset:3072
	ds_read_b128 v[170:173], v139 offset:4096
	ds_read_b128 v[174:177], v139 offset:5120
	ds_read_b128 v[178:181], v139 offset:6144
	ds_read_b128 v[182:185], v139 offset:7168
	s_cmp_eq_u32 s73, 1
	s_cbranch_scc1 .Lnd_proj_2
	global_load_lds_dwordx4 v[108:109], off
	v_lshl_add_u64 v[108:109], v[186:187], 0, s[22:23]
	s_mov_b32 m0, s57
	s_nop 0
	global_load_lds_dwordx4 v[108:109], off
.Lnd_proj_2:
	s_barrier
	s_waitcnt lgkmcnt(0)
	s_setprio 1
	s_waitcnt lgkmcnt(0)
	v_mfma_f32_16x16x32_f16 v[94:97], v[130:133], v[154:157], v[94:97]
	v_mfma_f32_16x16x32_f16 v[90:93], v[146:149], v[154:157], v[90:93]
	v_mfma_f32_16x16x32_f16 v[82:85], v[130:133], v[162:165], v[82:85]
	v_mfma_f32_16x16x32_f16 v[78:81], v[146:149], v[162:165], v[78:81]
	v_mfma_f32_16x16x32_f16 v[70:73], v[130:133], v[170:173], v[70:73]
	v_mfma_f32_16x16x32_f16 v[66:69], v[146:149], v[170:173], v[66:69]
	v_mfma_f32_16x16x32_f16 v[58:61], v[130:133], v[178:181], v[58:61]
	v_mfma_f32_16x16x32_f16 v[54:57], v[146:149], v[178:181], v[54:57]
	v_mfma_f32_16x16x32_f16 v[94:97], v[142:145], v[158:161], v[94:97]
	v_mfma_f32_16x16x32_f16 v[90:93], v[150:153], v[158:161], v[90:93]
	v_mfma_f32_16x16x32_f16 v[82:85], v[142:145], v[166:169], v[82:85]
	v_mfma_f32_16x16x32_f16 v[78:81], v[150:153], v[166:169], v[78:81]
	v_mfma_f32_16x16x32_f16 v[70:73], v[142:145], v[174:177], v[70:73]
	v_mfma_f32_16x16x32_f16 v[66:69], v[150:153], v[174:177], v[66:69]
	v_mfma_f32_16x16x32_f16 v[58:61], v[142:145], v[182:185], v[58:61]
	v_mfma_f32_16x16x32_f16 v[54:57], v[150:153], v[182:185], v[54:57]
	s_setprio 0
	s_barrier
	s_mov_b32 m0, s58
	v_lshl_add_u64 v[108:109], v[188:189], 0, s[22:23]
	ds_read_b128 v[130:133], v138 offset:4096
	ds_read_b128 v[142:145], v138 offset:5120
	s_cmp_eq_u32 s73, 1
	s_cbranch_scc1 .Lnd_proj_3
	global_load_lds_dwordx4 v[108:109], off
	v_lshl_add_u64 v[108:109], v[190:191], 0, s[22:23]
	s_add_i32 m0, s58, 0x2000
	s_nop 0
	global_load_lds_dwordx4 v[108:109], off
	v_lshl_add_u64 v[108:109], v[192:193], 0, s[22:23]
	s_add_i32 m0, s58, 0x4000
	s_nop 0
	global_load_lds_dwordx4 v[108:109], off
.Lnd_proj_3b:
	s_cmp_lg_u32 s67, 0
	s_cbranch_scc1 .Lpj_norm_2
	global_load_dwordx4 v[34:37], v[198:199], off offset:128
	global_load_dwordx4 v[38:41], v[200:201], off
	global_load_dwordx4 v[42:45], v[200:201], off offset:64
	global_load_dwordx4 v[46:49], v[200:201], off offset:128
	s_waitcnt vmcnt(13)
	s_branch .Lpj_join_2

.Lpj_join_2:
	s_barrier
	s_waitcnt lgkmcnt(0)
	s_setprio 1
	s_waitcnt lgkmcnt(0)
	v_mfma_f32_16x16x32_f16 v[86:89], v[130:133], v[154:157], v[86:89]
	v_mfma_f32_16x16x32_f16 v[74:77], v[130:133], v[162:165], v[74:77]
	v_mfma_f32_16x16x32_f16 v[62:65], v[130:133], v[170:173], v[62:65]
	v_mfma_f32_16x16x32_f16 v[50:53], v[130:133], v[178:181], v[50:53]
	v_mfma_f32_16x16x32_f16 v[86:89], v[142:145], v[158:161], v[86:89]
	v_mfma_f32_16x16x32_f16 v[74:77], v[142:145], v[166:169], v[74:77]
	v_mfma_f32_16x16x32_f16 v[62:65], v[142:145], v[174:177], v[62:65]
	v_mfma_f32_16x16x32_f16 v[50:53], v[142:145], v[182:185], v[50:53]
	s_setprio 0
	s_barrier
	s_add_i32 s67, s67, 3
	s_add_u32 s30, s30, 0x180
	s_addc_u32 s31, s31, 0
	s_cmp_ge_i32 s67, s59
	s_cbranch_scc0 .LBB4_22
	s_branch .LBB4_23
.Lnd_proj_3:
	s_waitcnt vmcnt(0)
	s_branch .Lnd_proj_3b

.LBB6_22:
	s_add_u32 s30, s22, s28
	s_addc_u32 s31, s23, s29
	s_add_u32 s30, s30, 0x180
	s_addc_u32 s31, s31, 0
	s_add_u32 s66, s24, s28
	s_addc_u32 s67, s25, s29
	s_add_u32 s68, s66, 0x180
	s_addc_u32 s69, s67, 0
	s_cmp_eq_u32 s60, s65
	s_cselect_b32 s67, s27, s31
	s_cselect_b32 s66, s26, s30
	s_cselect_b32 s31, s5, s69
	s_cselect_b32 s30, s4, s68
	s_cselect_b32 s71, 1, 0
	s_add_i32 s68, s62, s42
	v_add_u32_e32 v131, 0, v128
	v_add_u32_e32 v182, 0, v127
	v_lshl_add_u64 v[180:181], v[116:117], 0, s[28:29]
	s_mov_b32 m0, s68
	ds_read_b128 v[132:135], v131 offset:16384
	ds_read_b128 v[136:139], v131 offset:17408
	ds_read_b128 v[140:143], v131 offset:18432
	ds_read_b128 v[144:147], v131 offset:19456
	ds_read_b128 v[148:151], v182
	ds_read_b128 v[152:155], v182 offset:1024
	ds_read_b128 v[156:159], v182 offset:2048
	ds_read_b128 v[160:163], v182 offset:3072
	ds_read_b128 v[164:167], v182 offset:4096
	ds_read_b128 v[168:171], v182 offset:5120
	ds_read_b128 v[172:175], v182 offset:6144
	ds_read_b128 v[176:179], v182 offset:7168
	global_load_lds_dwordx4 v[180:181], off
	v_lshl_add_u64 v[180:181], v[118:119], 0, s[28:29]
	s_add_i32 m0, s68, 0x2000
	s_nop 0
	global_load_lds_dwordx4 v[180:181], off
	s_barrier
	s_waitcnt lgkmcnt(0)
	s_setprio 1
	s_waitcnt lgkmcnt(0)
	v_mfma_f32_16x16x32_f16 v[40:43], v[132:135], v[148:151], v[40:43]
	v_mfma_f32_16x16x32_f16 v[44:47], v[140:143], v[148:151], v[44:47]
	v_mfma_f32_16x16x32_f16 v[32:35], v[132:135], v[156:159], v[32:35]
	v_mfma_f32_16x16x32_f16 v[28:31], v[140:143], v[156:159], v[28:31]
	v_mfma_f32_16x16x32_f16 v[20:23], v[132:135], v[164:167], v[20:23]
	v_mfma_f32_16x16x32_f16 v[16:19], v[140:143], v[164:167], v[16:19]
	v_mfma_f32_16x16x32_f16 v[8:11], v[132:135], v[172:175], v[8:11]
	v_mfma_f32_16x16x32_f16 v[4:7], v[140:143], v[172:175], v[4:7]
	v_mfma_f32_16x16x32_f16 v[40:43], v[136:139], v[152:155], v[40:43]
	v_mfma_f32_16x16x32_f16 v[44:47], v[144:147], v[152:155], v[44:47]
	v_mfma_f32_16x16x32_f16 v[32:35], v[136:139], v[160:163], v[32:35]
	v_mfma_f32_16x16x32_f16 v[28:31], v[144:147], v[160:163], v[28:31]
	v_mfma_f32_16x16x32_f16 v[20:23], v[136:139], v[168:171], v[20:23]
	v_mfma_f32_16x16x32_f16 v[16:19], v[144:147], v[168:171], v[16:19]
	v_mfma_f32_16x16x32_f16 v[8:11], v[136:139], v[176:179], v[8:11]
	v_mfma_f32_16x16x32_f16 v[4:7], v[144:147], v[176:179], v[4:7]
	s_setprio 0
	s_barrier
	v_lshl_add_u64 v[140:141], v[120:121], 0, s[28:29]
	s_add_i32 m0, s47, 0x18000
	ds_read_b128 v[132:135], v131 offset:20480
	ds_read_b128 v[136:139], v131 offset:21504
	global_load_lds_dwordx4 v[140:141], off
	v_lshl_add_u64 v[140:141], v[122:123], 0, s[28:29]
	s_add_i32 m0, s47, 0x1a000
	s_nop 0
	global_load_lds_dwordx4 v[140:141], off
	v_lshl_add_u64 v[140:141], v[124:125], 0, s[28:29]
	s_add_i32 m0, s47, 0x1c000
	s_nop 0
	global_load_lds_dwordx4 v[140:141], off
	s_cmp_lg_u32 s65, 0
	s_cbranch_scc1 .Lm2_norm_0
	s_mul_i32 s70, s58, 0xc0
	v_add_u32_e32 v234, s70, v129
	v_ashrrev_i32_e32 v235, 31, v234
	v_lshlrev_b64 v[234:235], 2, v[234:235]
	v_lshl_add_u64 v[234:235], s[18:19], 0, v[234:235]
	global_load_dwordx4 v[222:225], v[234:235], off
	global_load_dwordx4 v[226:229], v[234:235], off offset:64
	global_load_dwordx4 v[230:233], v[234:235], off offset:128
	global_load_dwordx2 v[198:199], v[190:191], off
	global_load_dwordx2 v[200:201], v[190:191], off offset:32
	global_load_dwordx2 v[202:203], v[190:191], off offset:64
	global_load_dwordx2 v[204:205], v[192:193], off
	s_waitcnt vmcnt(12)
	s_branch .Lm2_join_0

.Lm2_join_0:
	s_barrier
	s_waitcnt lgkmcnt(0)
	s_setprio 1
	s_waitcnt lgkmcnt(0)
	v_mfma_f32_16x16x32_f16 v[36:39], v[132:135], v[148:151], v[36:39]
	v_mfma_f32_16x16x32_f16 v[24:27], v[132:135], v[156:159], v[24:27]
	v_mfma_f32_16x16x32_f16 v[12:15], v[132:135], v[164:167], v[12:15]
	v_mfma_f32_16x16x32_f16 v[0:3], v[132:135], v[172:175], v[0:3]
	v_mfma_f32_16x16x32_f16 v[36:39], v[136:139], v[152:155], v[36:39]
	v_mfma_f32_16x16x32_f16 v[24:27], v[136:139], v[160:163], v[24:27]
	v_mfma_f32_16x16x32_f16 v[12:15], v[136:139], v[168:171], v[12:15]
	v_mfma_f32_16x16x32_f16 v[0:3], v[136:139], v[176:179], v[0:3]
	s_setprio 0
	s_barrier
	s_mov_b32 m0, s47
	v_lshl_add_u64 v[180:181], s[66:67], 0, v[48:49]
	ds_read_b128 v[132:135], v131 offset:57344
	ds_read_b128 v[136:139], v131 offset:58368
	ds_read_b128 v[140:143], v131 offset:59392
	ds_read_b128 v[144:147], v131 offset:60416
	ds_read_b128 v[148:151], v182 offset:40960
	ds_read_b128 v[152:155], v182 offset:41984
	ds_read_b128 v[156:159], v182 offset:43008
	ds_read_b128 v[160:163], v182 offset:44032
	ds_read_b128 v[164:167], v182 offset:45056
	ds_read_b128 v[168:171], v182 offset:46080
	ds_read_b128 v[172:175], v182 offset:47104
	ds_read_b128 v[176:179], v182 offset:48128
	s_cmp_eq_u32 s71, 1
	s_cbranch_scc1 .Lnd_mlp2_0
	global_load_lds_dwordx4 v[180:181], off
	v_lshl_add_u64 v[182:183], s[66:67], 0, v[52:53]
	s_mov_b32 m0, s48
	s_nop 0
	global_load_lds_dwordx4 v[182:183], off
.Lnd_mlp2_0:
	s_barrier
	s_waitcnt lgkmcnt(0)
	s_setprio 1
	s_waitcnt lgkmcnt(0)
	v_mfma_f32_16x16x32_f16 v[40:43], v[132:135], v[148:151], v[40:43]
	v_mfma_f32_16x16x32_f16 v[44:47], v[140:143], v[148:151], v[44:47]
	v_mfma_f32_16x16x32_f16 v[32:35], v[132:135], v[156:159], v[32:35]
	v_mfma_f32_16x16x32_f16 v[28:31], v[140:143], v[156:159], v[28:31]
	v_mfma_f32_16x16x32_f16 v[20:23], v[132:135], v[164:167], v[20:23]
	v_mfma_f32_16x16x32_f16 v[16:19], v[140:143], v[164:167], v[16:19]
	v_mfma_f32_16x16x32_f16 v[8:11], v[132:135], v[172:175], v[8:11]
	v_mfma_f32_16x16x32_f16 v[4:7], v[140:143], v[172:175], v[4:7]
	v_mfma_f32_16x16x32_f16 v[40:43], v[136:139], v[152:155], v[40:43]
	v_mfma_f32_16x16x32_f16 v[44:47], v[144:147], v[152:155], v[44:47]
	v_mfma_f32_16x16x32_f16 v[32:35], v[136:139], v[160:163], v[32:35]
	v_mfma_f32_16x16x32_f16 v[28:31], v[144:147], v[160:163], v[28:31]
	v_mfma_f32_16x16x32_f16 v[20:23], v[136:139], v[168:171], v[20:23]
	v_mfma_f32_16x16x32_f16 v[16:19], v[144:147], v[168:171], v[16:19]
	v_mfma_f32_16x16x32_f16 v[8:11], v[136:139], v[176:179], v[8:11]
	v_mfma_f32_16x16x32_f16 v[4:7], v[144:147], v[176:179], v[4:7]
	s_setprio 0
	s_barrier
	s_mov_b32 m0, s49
	v_lshl_add_u64 v[184:185], s[30:31], 0, v[50:51]
	ds_read_b128 v[132:135], v131 offset:61440
	ds_read_b128 v[136:139], v131 offset:62464
	s_cmp_eq_u32 s71, 1
	s_cbranch_scc1 .Lnd_mlp2_1
	global_load_lds_dwordx4 v[184:185], off
	v_lshl_add_u64 v[186:187], s[30:31], 0, v[54:55]
	s_mov_b32 m0, s50
	v_lshl_add_u64 v[188:189], s[30:31], 0, v[56:57]
	global_load_lds_dwordx4 v[186:187], off
	s_mov_b32 m0, s51
	s_nop 0
	global_load_lds_dwordx4 v[188:189], off
.Lnd_mlp2_1b:
	s_cmp_lg_u32 s65, 0
	s_cbranch_scc1 .Lm2_norm_1
	global_load_dwordx2 v[206:207], v[192:193], off offset:32
	global_load_dwordx2 v[208:209], v[192:193], off offset:64
	global_load_dwordx2 v[210:211], v[194:195], off
	global_load_dwordx2 v[212:213], v[194:195], off offset:32
	s_waitcnt vmcnt(16)
	s_branch .Lm2_join_1

.Lm2_join_1:
	s_barrier
	s_waitcnt lgkmcnt(0)
	s_setprio 1
	s_waitcnt lgkmcnt(0)
	v_mfma_f32_16x16x32_f16 v[36:39], v[132:135], v[148:151], v[36:39]
	v_mfma_f32_16x16x32_f16 v[24:27], v[132:135], v[156:159], v[24:27]
	v_mfma_f32_16x16x32_f16 v[12:15], v[132:135], v[164:167], v[12:15]
	v_mfma_f32_16x16x32_f16 v[0:3], v[132:135], v[172:175], v[0:3]
	v_mfma_f32_16x16x32_f16 v[36:39], v[136:139], v[152:155], v[36:39]
	v_mfma_f32_16x16x32_f16 v[24:27], v[136:139], v[160:163], v[24:27]
	v_mfma_f32_16x16x32_f16 v[12:15], v[136:139], v[168:171], v[12:15]
	v_mfma_f32_16x16x32_f16 v[0:3], v[136:139], v[176:179], v[0:3]
	s_setprio 0
	s_barrier
	s_mov_b32 m0, s54
	v_add_u32_e32 v131, s62, v127
	v_lshl_add_u64 v[180:181], v[180:181], 0, s[20:21]
	ds_read_b128 v[132:135], v130
	ds_read_b128 v[136:139], v130 offset:1024
	ds_read_b128 v[140:143], v130 offset:2048
	ds_read_b128 v[144:147], v130 offset:3072
	ds_read_b128 v[148:151], v131
	ds_read_b128 v[152:155], v131 offset:1024
	ds_read_b128 v[156:159], v131 offset:2048
	ds_read_b128 v[160:163], v131 offset:3072
	ds_read_b128 v[164:167], v131 offset:4096
	ds_read_b128 v[168:171], v131 offset:5120
	ds_read_b128 v[172:175], v131 offset:6144
	ds_read_b128 v[176:179], v131 offset:7168
	s_cmp_eq_u32 s71, 1
	s_cbranch_scc1 .Lnd_mlp2_2
	global_load_lds_dwordx4 v[180:181], off
	v_lshl_add_u64 v[180:181], v[182:183], 0, s[20:21]
	s_mov_b32 m0, s55
	s_nop 0
	global_load_lds_dwordx4 v[180:181], off
.Lnd_mlp2_2:
	s_barrier
	s_waitcnt lgkmcnt(0)
	s_setprio 1
	s_waitcnt lgkmcnt(0)
	v_mfma_f32_16x16x32_f16 v[40:43], v[132:135], v[148:151], v[40:43]
	v_mfma_f32_16x16x32_f16 v[44:47], v[140:143], v[148:151], v[44:47]
	v_mfma_f32_16x16x32_f16 v[32:35], v[132:135], v[156:159], v[32:35]
	v_mfma_f32_16x16x32_f16 v[28:31], v[140:143], v[156:159], v[28:31]
	v_mfma_f32_16x16x32_f16 v[20:23], v[132:135], v[164:167], v[20:23]
	v_mfma_f32_16x16x32_f16 v[16:19], v[140:143], v[164:167], v[16:19]
	v_mfma_f32_16x16x32_f16 v[8:11], v[132:135], v[172:175], v[8:11]
	v_mfma_f32_16x16x32_f16 v[4:7], v[140:143], v[172:175], v[4:7]
	v_mfma_f32_16x16x32_f16 v[40:43], v[136:139], v[152:155], v[40:43]
	v_mfma_f32_16x16x32_f16 v[44:47], v[144:147], v[152:155], v[44:47]
	v_mfma_f32_16x16x32_f16 v[32:35], v[136:139], v[160:163], v[32:35]
	v_mfma_f32_16x16x32_f16 v[28:31], v[144:147], v[160:163], v[28:31]
	v_mfma_f32_16x16x32_f16 v[20:23], v[136:139], v[168:171], v[20:23]
	v_mfma_f32_16x16x32_f16 v[16:19], v[144:147], v[168:171], v[16:19]
	v_mfma_f32_16x16x32_f16 v[8:11], v[136:139], v[176:179], v[8:11]
	v_mfma_f32_16x16x32_f16 v[4:7], v[144:147], v[176:179], v[4:7]
	s_setprio 0
	s_barrier
	s_mov_b32 m0, s56
	v_lshl_add_u64 v[140:141], v[184:185], 0, s[20:21]
	ds_read_b128 v[132:135], v130 offset:4096
	ds_read_b128 v[136:139], v130 offset:5120
	s_cmp_eq_u32 s71, 1
	s_cbranch_scc1 .Lnd_mlp2_3
	global_load_lds_dwordx4 v[140:141], off
	v_lshl_add_u64 v[140:141], v[186:187], 0, s[20:21]
	s_add_i32 m0, s56, 0x2000
	s_nop 0
	global_load_lds_dwordx4 v[140:141], off
	v_lshl_add_u64 v[140:141], v[188:189], 0, s[20:21]
	s_add_i32 m0, s56, 0x4000
	s_nop 0
	global_load_lds_dwordx4 v[140:141], off
.Lnd_mlp2_3b:
	s_cmp_lg_u32 s65, 0
	s_cbranch_scc1 .Lm2_norm_2
	global_load_dwordx2 v[214:215], v[194:195], off offset:64
	global_load_dwordx2 v[216:217], v[196:197], off
	global_load_dwordx2 v[218:219], v[196:197], off offset:32
	global_load_dwordx2 v[220:221], v[196:197], off offset:64
	s_waitcnt vmcnt(13)
	s_branch .Lm2_join_2
